# speedup vs baseline: 1.0126x; 1.0118x over previous
.Lm_nok_p1:
	s_waitcnt vmcnt(2)
	s_nop 0
	v_max3_f32 v132, v132, v133, v134
	v_max3_f32 v136, v136, v137, v138
	v_max3_f32 v132, v132, v135, v139
	v_max3_f32 v132, v132, v136, v140
	s_nop 1
	v_max_f32_dpp v132, v132, v132 quad_perm:[1,0,3,2] row_mask:0xf bank_mask:0xf
	s_nop 1
	v_max_f32_dpp v132, v132, v132 quad_perm:[2,3,0,1] row_mask:0xf bank_mask:0xf
	s_nop 1
	v_max_f32_dpp v132, v132, v132 row_half_mirror row_mask:0xf bank_mask:0xf
	s_nop 1
	v_max_f32_dpp v132, v132, v132 row_mirror row_mask:0xf bank_mask:0xf
	s_nop 1
	v_readlane_b32 s36, v132, 0
	v_readlane_b32 s37, v132, 16
	v_readlane_b32 s38, v132, 32
	v_readlane_b32 s39, v132, 48
	s_nop 2
	v_mov_b32_e32 v133, s36
	v_max_f32_e32 v133, s37, v133
	v_max_f32_e32 v133, s38, v133
	v_max_f32_e32 v133, s39, v133
	s_mov_b32 s37, 0xf800000
	v_mul_f32_e32 v137, 0x4f800000, v133
	v_cmp_gt_f32_e32 vcc, s37, v133
	s_nop 1
	v_cndmask_b32_e32 v133, v133, v137, vcc
	v_sqrt_f32_e32 v137, v133
	s_nop 0
	v_add_u32_e32 v138, -1, v137
	v_add_u32_e32 v139, 1, v137
	v_fma_f32 v143, -v138, v137, v133
	v_fma_f32 v144, -v139, v137, v133
	v_cmp_ge_f32_e64 s[38:39], 0, v143
	s_nop 1
	v_cndmask_b32_e64 v137, v137, v138, s[38:39]
	v_cmp_lt_f32_e64 s[38:39], 0, v144
	s_nop 1
	v_cndmask_b32_e64 v137, v137, v139, s[38:39]
	v_mul_f32_e32 v138, 0x37800000, v137
	v_cndmask_b32_e32 v137, v137, v138, vcc
	v_mov_b32_e32 v138, 0x260
	v_cmp_class_f32_e32 vcc, v133, v138
	s_nop 1
	v_cndmask_b32_e32 v133, v137, v133, vcc
	v_mov_b32_e32 v135, 0x3ca3d70a
	s_mov_b32 s36, 0xffff
	v_mul_f32_e32 v134, v141, v133
	v_mul_f32_e32 v136, v142, v133
	v_fmamk_f32 v134, v134, 0x3f804189, v135
	v_fmamk_f32 v136, v136, 0x3f804189, v135
	v_cvt_f16_f32_e64 v134, -v134
	v_cvt_f16_f32_e64 v136, -v136
	v_cmp_gt_u32_e32 vcc, 32, v1
	v_cvt_f32_f16_e32 v148, v134
	v_cvt_f32_f16_e32 v149, v136
	v_bfi_b32 v134, s36, v134, v11
	v_bfi_b32 v136, s36, v136, v15
	v_cndmask_b32_e32 v11, v11, v134, vcc
	v_cndmask_b32_e32 v15, v15, v136, vcc
	v_mov_b32_e32 v16, 0
	v_mov_b32_e32 v17, 0
	v_mov_b32_e32 v18, 0
	v_mov_b32_e32 v19, 0
	v_mov_b32_e32 v20, 0
	v_mov_b32_e32 v21, 0
	v_mov_b32_e32 v22, 0
	v_mov_b32_e32 v23, 0
	v_mov_b32_e32 v24, 0
	v_mov_b32_e32 v25, 0
	v_mov_b32_e32 v26, 0
	v_mov_b32_e32 v27, 0
	v_mov_b32_e32 v28, 0
	v_mov_b32_e32 v29, 0
	v_mov_b32_e32 v30, 0
	v_mov_b32_e32 v31, 0
	v_mov_b32_e32 v32, 0
	v_mov_b32_e32 v33, 0
	v_mov_b32_e32 v34, 0
	v_mov_b32_e32 v35, 0
	v_mov_b32_e32 v36, 0
	v_mov_b32_e32 v37, 0
	v_mov_b32_e32 v38, 0
	v_mov_b32_e32 v39, 0
	v_mov_b32_e32 v40, 0
	v_mov_b32_e32 v41, 0
	v_mov_b32_e32 v42, 0
	v_mov_b32_e32 v43, 0
	v_mov_b32_e32 v44, 0
	v_mov_b32_e32 v45, 0
	v_mov_b32_e32 v46, 0
	v_mov_b32_e32 v47, 0
	s_waitcnt vmcnt(0)
	s_barrier
	s_mov_b32 s28, 2
	v_add_u32_e32 v128, s46, v2
	v_add_u32_e32 v129, s47, v2
	ds_read_b128 v[88:91], v128 offset:24576
	ds_read_b128 v[92:95], v128 offset:25600
	ds_read_b128 v[96:99], v128 offset:0
	ds_read_b128 v[104:107], v128 offset:2048
	ds_read_b128 v[100:103], v128 offset:1024
	ds_read_b128 v[108:111], v128 offset:3072
	s_sub_u32 s30, s28, s25
	s_mul_i32 s30, s30, 6
	s_add_u32 s30, s30, s24
	s_mul_i32 s31, s28, 6
	s_add_u32 s31, s31, s22
	s_cmp_lt_u32 s28, s25
	s_cselect_b32 s30, s31, s30
	s_lshl_b32 s33, s18, 10
	s_lshl_b32 s31, s30, 12
	s_add_u32 s31, s31, s33
	s_add_u32 s50, s8, s31
	s_addc_u32 s51, s9, 0
	s_add_u32 s52, s50, 0x3000
	s_addc_u32 s53, s51, 0
	s_add_u32 s34, s48, s33
	s_mov_b32 m0, s34
	s_add_u32 s35, s34, 0x3000
	global_load_lds_dwordx4 v2, s[50:51]
	s_mov_b32 m0, s35
	s_nop 0
	global_load_lds_dwordx4 v2, s[52:53]
	s_cmp_lt_u32 s18, 6
	s_cbranch_scc0 .Lm_nok_p2
	s_lshl_b32 s31, s30, 10
	s_add_u32 s31, s31, s33
	s_add_u32 s54, s4, s31
	s_addc_u32 s55, s5, 0
	s_add_u32 s34, s34, 24576
	s_mov_b32 m0, s34
	s_nop 0
	global_load_lds_dwordx4 v2, s[54:55]
.Lm_nok_p2:
	s_waitcnt lgkmcnt(5)
	v_mfma_f32_32x32x16_f16 v[48:63], v[88:91], v[8:11], 0
	s_nop 5
	s_waitcnt lgkmcnt(4)
	v_mfma_f32_32x32x16_f16 v[64:79], v[92:95], v[8:11], 0
	ds_read_b128 v[88:91], v128 offset:26624
	ds_read_b128 v[112:115], v128 offset:4096
	ds_read_b128 v[120:123], v128 offset:6144
	v_exp_f32_e32 v48, v48
	v_exp_f32_e32 v49, v49
	v_exp_f32_e32 v50, v50
	v_exp_f32_e32 v51, v51
	v_exp_f32_e32 v52, v52
	v_exp_f32_e32 v53, v53
	v_exp_f32_e32 v54, v54
	v_exp_f32_e32 v55, v55
	v_cvt_pk_bf16_f32 v80, v48, v49
	v_cvt_pk_bf16_f32 v81, v50, v51
	v_cvt_pk_bf16_f32 v82, v52, v53
	v_cvt_pk_bf16_f32 v83, v54, v55
	ds_read_b128 v[116:119], v128 offset:5120
	ds_read_b128 v[124:127], v128 offset:7168
	v_exp_f32_e32 v56, v56
	v_exp_f32_e32 v57, v57
	v_exp_f32_e32 v58, v58
	v_exp_f32_e32 v59, v59
	s_waitcnt lgkmcnt(7)
	v_mfma_f32_32x32x16_bf16 v[16:31], v[96:99], v[80:83], v[16:31]
	v_exp_f32_e32 v60, v60
	v_exp_f32_e32 v61, v61
	v_exp_f32_e32 v62, v62
	v_exp_f32_e32 v63, v63
	v_mfma_f32_32x32x16_bf16 v[32:47], v[104:107], v[80:83], v[32:47]
	v_cvt_pk_bf16_f32 v84, v56, v57
	v_cvt_pk_bf16_f32 v85, v58, v59
	v_cvt_pk_bf16_f32 v86, v60, v61
	v_cvt_pk_bf16_f32 v87, v62, v63
	s_branch .Lm_steps1

.Lm_flush:
	s_nop 15
	v_div_scale_f32 v132, s[30:31], v42, v42, 1.0
	v_rcp_f32_e32 v133, v132
	v_div_scale_f32 v134, vcc, 1.0, v42, 1.0
	v_fma_f32 v135, -v132, v133, 1.0
	v_fmac_f32_e32 v133, v135, v133
	v_mul_f32_e32 v135, v134, v133
	v_fma_f32 v136, -v132, v135, v134
	v_fmac_f32_e32 v135, v136, v133
	v_fma_f32 v132, -v132, v135, v134
	s_mul_i32 s40, s29, 0x180
	s_lshl_b32 s41, s18, 5
	v_div_fmas_f32 v132, v132, v133, v135
	v_div_fixup_f32 v132, v132, v42, 1.0
	v_cmp_lt_f32_e32 vcc, 0, v42
	s_add_u32 s40, s40, s41
	s_lshl_b32 s44, s40, 2
	s_mul_i32 s45, s40, 0x68
	s_add_u32 s42, s16, s44
	s_addc_u32 s43, s17, 0
	v_cndmask_b32_e32 v130, 0, v132, vcc
	s_add_u32 s40, s14, s45
	s_addc_u32 s41, s15, 0
	v_mov_b32_e32 v131, v130
	v_pk_mul_f32 v[132:133], v[16:17], v[130:131]
	v_pk_mul_f32 v[134:135], v[18:19], v[130:131]
	v_cvt_pk_f16_f32 v136, v132, v133
	v_cvt_pk_f16_f32 v137, v134, v135
	ds_write_b64 v6, v[136:137] offset:0
	v_pk_mul_f32 v[132:133], v[20:21], v[130:131]
	v_pk_mul_f32 v[134:135], v[22:23], v[130:131]
	v_cvt_pk_f16_f32 v136, v132, v133
	v_cvt_pk_f16_f32 v137, v134, v135
	ds_write_b64 v6, v[136:137] offset:16
	v_pk_mul_f32 v[132:133], v[24:25], v[130:131]
	v_pk_mul_f32 v[134:135], v[26:27], v[130:131]
	v_cvt_pk_f16_f32 v136, v132, v133
	v_cvt_pk_f16_f32 v137, v134, v135
	ds_write_b64 v6, v[136:137] offset:32
	v_pk_mul_f32 v[132:133], v[28:29], v[130:131]
	v_pk_mul_f32 v[134:135], v[30:31], v[130:131]
	v_cvt_pk_f16_f32 v136, v132, v133
	v_cvt_pk_f16_f32 v137, v134, v135
	ds_write_b64 v6, v[136:137] offset:48
	v_pk_mul_f32 v[132:133], v[32:33], v[130:131]
	v_pk_mul_f32 v[134:135], v[34:35], v[130:131]
	v_cvt_pk_f16_f32 v136, v132, v133
	v_cvt_pk_f16_f32 v137, v134, v135
	ds_write_b64 v6, v[136:137] offset:64
	v_pk_mul_f32 v[132:133], v[36:37], v[130:131]
	v_pk_mul_f32 v[134:135], v[38:39], v[130:131]
	v_cvt_pk_f16_f32 v136, v132, v133
	v_cvt_pk_f16_f32 v137, v134, v135
	ds_write_b64 v6, v[136:137] offset:80
	s_mov_b32 exec_hi, 0
	v_pk_mul_f32 v[132:133], v[40:41], v[130:131]
	v_pk_mul_f32 v[134:135], v[42:43], v[130:131]
	v_cvt_pk_f16_f32 v136, v132, v133
	v_cvt_pk_f16_f32 v137, v134, v135
	ds_write_b64 v6, v[136:137] offset:96
	s_mov_b64 exec, -1
	s_waitcnt lgkmcnt(0)
	ds_read_b128 v[132:135], v7 offset:0
	ds_read_b128 v[136:139], v7 offset:1024
	ds_read_b128 v[140:143], v7 offset:2048
	ds_read_b128 v[144:147], v7 offset:3072
	v_log_f32_e32 v131, v42
	s_waitcnt lgkmcnt(0)
	v_sub_f32_e32 v131, v131, v148
	global_store_dwordx4 v2, v[132:135], s[40:41] offset:0 nt
	global_store_dwordx4 v2, v[136:139], s[40:41] offset:1024 nt
	global_store_dwordx4 v2, v[140:143], s[40:41] offset:2048 nt
	v_cndmask_b32_e32 v131, v150, v131, vcc
	s_mov_b32 exec_lo, 0xffff
	s_mov_b32 exec_hi, 0
	global_store_dwordx4 v2, v[144:147], s[40:41] offset:3072 nt
	s_mov_b32 exec_lo, -1
	global_store_dword v5, v131, s[42:43]
	s_mov_b64 exec, -1
	s_cmp_lt_u32 s27, 9
	s_cbranch_scc1 .Lm_switch
	s_endpgm
